# speedup vs baseline: 1.0345x; 1.0032x over previous
.LBB1_27:
	s_and_b64 vcc, exec, s[4:5]
	s_cbranch_vccz .LBB1_32
	s_sub_i32 s3, s2, 0x100
	s_cmp_gt_u32 s3, 0xf9
	s_cbranch_scc1 .LBB1_32
	s_load_dwordx4 s[4:7], s[0:1], 0x20
	s_load_dwordx2 s[8:9], s[0:1], 0x30
	s_load_dwordx4 s[12:15], s[0:1], 0x38
	v_lshrrev_b32_e32 v46, 3, v0
	v_and_b32_e32 v47, 7, v0
	v_and_b32_e32 v50, 7, v46
	v_lshrrev_b32_e32 v51, 3, v46
	v_and_b32_e32 v52, 3, v51
	v_lshrrev_b32_e32 v51, 2, v51
	v_lshlrev_b32_e32 v50, 2, v50
	v_lshl_add_u32 v50, v51, 5, v50
	v_add_u32_e32 v50, v50, v52
	v_and_b32_e32 v51, 7, v50
	v_lshrrev_b32_e32 v50, 3, v50
	v_lshl_add_u32 v50, v51, 4, v50
	v_lshl_add_u32 v50, v50, 3, v47
	v_lshlrev_b32_e32 v44, 2, v50
	v_readfirstlane_b32 s16, v0
	s_mul_i32 s3, s3, 0x50
	v_lshlrev_b32_e32 v49, 5, v47
	v_lshlrev_b32_e32 v53, 2, v0
	s_waitcnt lgkmcnt(0)
	global_load_dword v45, v44, s[6:7]
	s_cmp_ge_u32 s16, 0x280
	s_cbranch_scc1 .Lkb_nd_fill
	v_add_u32_e32 v46, s3, v46
	v_lshlrev_b32_e32 v48, 9, v46
	v_lshl_add_u32 v48, v47, 4, v48
	global_load_dwordx4 v[2:5], v48, s[4:5] offset:0
	global_load_dwordx4 v[6:9], v48, s[4:5] offset:128
	global_load_dwordx4 v[10:13], v48, s[4:5] offset:256
	global_load_dwordx4 v[14:17], v48, s[4:5] offset:384
	s_waitcnt vmcnt(4)
	ds_write_b32 v53, v45
	s_waitcnt lgkmcnt(0)
	s_barrier
	ds_read_b128 v[26:29], v49 offset:0
	ds_read_b128 v[30:33], v49 offset:16
	ds_read_b128 v[34:37], v49 offset:256
	ds_read_b128 v[38:41], v49 offset:272
	v_lshlrev_b32_e32 v54, 8, v46
	v_lshl_add_u32 v54, v47, 3, v54
	s_waitcnt vmcnt(0)
	v_cvt_pk_f16_f32 v50, v2, v3
	v_cvt_pk_f16_f32 v51, v4, v5
	global_store_dwordx2 v54, v[50:51], s[8:9] offset:0
	v_cvt_pk_f16_f32 v52, v6, v7
	v_cvt_pk_f16_f32 v53, v8, v9
	global_store_dwordx2 v54, v[52:53], s[8:9] offset:64
	v_cvt_pk_f16_f32 v50, v10, v11
	v_cvt_pk_f16_f32 v51, v12, v13
	global_store_dwordx2 v54, v[50:51], s[8:9] offset:128
	v_cvt_pk_f16_f32 v52, v14, v15
	v_cvt_pk_f16_f32 v53, v16, v17
	global_store_dwordx2 v54, v[52:53], s[8:9] offset:192
	s_waitcnt lgkmcnt(2)
	v_pk_mul_f32 v[18:19], v[2:3], v[26:27] op_sel_hi:[0,1]
	v_pk_mul_f32 v[20:21], v[2:3], v[28:29] op_sel_hi:[0,1]
	v_pk_mul_f32 v[22:23], v[2:3], v[30:31] op_sel_hi:[0,1]
	v_pk_mul_f32 v[24:25], v[2:3], v[32:33] op_sel_hi:[0,1]
	ds_read_b128 v[26:29], v49 offset:512
	ds_read_b128 v[30:33], v49 offset:528
	s_waitcnt lgkmcnt(2)
	v_pk_fma_f32 v[18:19], v[2:3], v[34:35], v[18:19] op_sel:[1,0,0]
	v_pk_fma_f32 v[20:21], v[2:3], v[36:37], v[20:21] op_sel:[1,0,0]
	v_pk_fma_f32 v[22:23], v[2:3], v[38:39], v[22:23] op_sel:[1,0,0]
	v_pk_fma_f32 v[24:25], v[2:3], v[40:41], v[24:25] op_sel:[1,0,0]
	ds_read_b128 v[34:37], v49 offset:768
	ds_read_b128 v[38:41], v49 offset:784
	s_waitcnt lgkmcnt(2)
	v_pk_fma_f32 v[18:19], v[4:5], v[26:27], v[18:19] op_sel_hi:[0,1,1]
	v_pk_fma_f32 v[20:21], v[4:5], v[28:29], v[20:21] op_sel_hi:[0,1,1]
	v_pk_fma_f32 v[22:23], v[4:5], v[30:31], v[22:23] op_sel_hi:[0,1,1]
	v_pk_fma_f32 v[24:25], v[4:5], v[32:33], v[24:25] op_sel_hi:[0,1,1]
	ds_read_b128 v[26:29], v49 offset:1024
	ds_read_b128 v[30:33], v49 offset:1040
	s_waitcnt lgkmcnt(2)
	v_pk_fma_f32 v[18:19], v[4:5], v[34:35], v[18:19] op_sel:[1,0,0]
	v_pk_fma_f32 v[20:21], v[4:5], v[36:37], v[20:21] op_sel:[1,0,0]
	v_pk_fma_f32 v[22:23], v[4:5], v[38:39], v[22:23] op_sel:[1,0,0]
	v_pk_fma_f32 v[24:25], v[4:5], v[40:41], v[24:25] op_sel:[1,0,0]
	ds_read_b128 v[34:37], v49 offset:1280
	ds_read_b128 v[38:41], v49 offset:1296
	s_waitcnt lgkmcnt(2)
	v_pk_fma_f32 v[18:19], v[6:7], v[26:27], v[18:19] op_sel_hi:[0,1,1]
	v_pk_fma_f32 v[20:21], v[6:7], v[28:29], v[20:21] op_sel_hi:[0,1,1]
	v_pk_fma_f32 v[22:23], v[6:7], v[30:31], v[22:23] op_sel_hi:[0,1,1]
	v_pk_fma_f32 v[24:25], v[6:7], v[32:33], v[24:25] op_sel_hi:[0,1,1]
	ds_read_b128 v[26:29], v49 offset:1536
	ds_read_b128 v[30:33], v49 offset:1552
	s_waitcnt lgkmcnt(2)
	v_pk_fma_f32 v[18:19], v[6:7], v[34:35], v[18:19] op_sel:[1,0,0]
	v_pk_fma_f32 v[20:21], v[6:7], v[36:37], v[20:21] op_sel:[1,0,0]
	v_pk_fma_f32 v[22:23], v[6:7], v[38:39], v[22:23] op_sel:[1,0,0]
	v_pk_fma_f32 v[24:25], v[6:7], v[40:41], v[24:25] op_sel:[1,0,0]
	ds_read_b128 v[34:37], v49 offset:1792
	ds_read_b128 v[38:41], v49 offset:1808
	s_waitcnt lgkmcnt(2)
	v_pk_fma_f32 v[18:19], v[8:9], v[26:27], v[18:19] op_sel_hi:[0,1,1]
	v_pk_fma_f32 v[20:21], v[8:9], v[28:29], v[20:21] op_sel_hi:[0,1,1]
	v_pk_fma_f32 v[22:23], v[8:9], v[30:31], v[22:23] op_sel_hi:[0,1,1]
	v_pk_fma_f32 v[24:25], v[8:9], v[32:33], v[24:25] op_sel_hi:[0,1,1]
	ds_read_b128 v[26:29], v49 offset:2048
	ds_read_b128 v[30:33], v49 offset:2064
	s_waitcnt lgkmcnt(2)
	v_pk_fma_f32 v[18:19], v[8:9], v[34:35], v[18:19] op_sel:[1,0,0]
	v_pk_fma_f32 v[20:21], v[8:9], v[36:37], v[20:21] op_sel:[1,0,0]
	v_pk_fma_f32 v[22:23], v[8:9], v[38:39], v[22:23] op_sel:[1,0,0]
	v_pk_fma_f32 v[24:25], v[8:9], v[40:41], v[24:25] op_sel:[1,0,0]
	ds_read_b128 v[34:37], v49 offset:2304
	ds_read_b128 v[38:41], v49 offset:2320
	s_waitcnt lgkmcnt(2)
	v_pk_fma_f32 v[18:19], v[10:11], v[26:27], v[18:19] op_sel_hi:[0,1,1]
	v_pk_fma_f32 v[20:21], v[10:11], v[28:29], v[20:21] op_sel_hi:[0,1,1]
	v_pk_fma_f32 v[22:23], v[10:11], v[30:31], v[22:23] op_sel_hi:[0,1,1]
	v_pk_fma_f32 v[24:25], v[10:11], v[32:33], v[24:25] op_sel_hi:[0,1,1]
	ds_read_b128 v[26:29], v49 offset:2560
	ds_read_b128 v[30:33], v49 offset:2576
	s_waitcnt lgkmcnt(2)
	v_pk_fma_f32 v[18:19], v[10:11], v[34:35], v[18:19] op_sel:[1,0,0]
	v_pk_fma_f32 v[20:21], v[10:11], v[36:37], v[20:21] op_sel:[1,0,0]
	v_pk_fma_f32 v[22:23], v[10:11], v[38:39], v[22:23] op_sel:[1,0,0]
	v_pk_fma_f32 v[24:25], v[10:11], v[40:41], v[24:25] op_sel:[1,0,0]
	ds_read_b128 v[34:37], v49 offset:2816
	ds_read_b128 v[38:41], v49 offset:2832
	s_waitcnt lgkmcnt(2)
	v_pk_fma_f32 v[18:19], v[12:13], v[26:27], v[18:19] op_sel_hi:[0,1,1]
	v_pk_fma_f32 v[20:21], v[12:13], v[28:29], v[20:21] op_sel_hi:[0,1,1]
	v_pk_fma_f32 v[22:23], v[12:13], v[30:31], v[22:23] op_sel_hi:[0,1,1]
	v_pk_fma_f32 v[24:25], v[12:13], v[32:33], v[24:25] op_sel_hi:[0,1,1]
	ds_read_b128 v[26:29], v49 offset:3072
	ds_read_b128 v[30:33], v49 offset:3088
	s_waitcnt lgkmcnt(2)
	v_pk_fma_f32 v[18:19], v[12:13], v[34:35], v[18:19] op_sel:[1,0,0]
	v_pk_fma_f32 v[20:21], v[12:13], v[36:37], v[20:21] op_sel:[1,0,0]
	v_pk_fma_f32 v[22:23], v[12:13], v[38:39], v[22:23] op_sel:[1,0,0]
	v_pk_fma_f32 v[24:25], v[12:13], v[40:41], v[24:25] op_sel:[1,0,0]
	ds_read_b128 v[34:37], v49 offset:3328
	ds_read_b128 v[38:41], v49 offset:3344
	s_waitcnt lgkmcnt(2)
	v_pk_fma_f32 v[18:19], v[14:15], v[26:27], v[18:19] op_sel_hi:[0,1,1]
	v_pk_fma_f32 v[20:21], v[14:15], v[28:29], v[20:21] op_sel_hi:[0,1,1]
	v_pk_fma_f32 v[22:23], v[14:15], v[30:31], v[22:23] op_sel_hi:[0,1,1]
	v_pk_fma_f32 v[24:25], v[14:15], v[32:33], v[24:25] op_sel_hi:[0,1,1]
	ds_read_b128 v[26:29], v49 offset:3584
	ds_read_b128 v[30:33], v49 offset:3600
	s_waitcnt lgkmcnt(2)
	v_pk_fma_f32 v[18:19], v[14:15], v[34:35], v[18:19] op_sel:[1,0,0]
	v_pk_fma_f32 v[20:21], v[14:15], v[36:37], v[20:21] op_sel:[1,0,0]
	v_pk_fma_f32 v[22:23], v[14:15], v[38:39], v[22:23] op_sel:[1,0,0]
	v_pk_fma_f32 v[24:25], v[14:15], v[40:41], v[24:25] op_sel:[1,0,0]
	ds_read_b128 v[34:37], v49 offset:3840
	ds_read_b128 v[38:41], v49 offset:3856
	s_waitcnt lgkmcnt(2)
	v_pk_fma_f32 v[18:19], v[16:17], v[26:27], v[18:19] op_sel_hi:[0,1,1]
	v_pk_fma_f32 v[20:21], v[16:17], v[28:29], v[20:21] op_sel_hi:[0,1,1]
	v_pk_fma_f32 v[22:23], v[16:17], v[30:31], v[22:23] op_sel_hi:[0,1,1]
	v_pk_fma_f32 v[24:25], v[16:17], v[32:33], v[24:25] op_sel_hi:[0,1,1]
	s_waitcnt lgkmcnt(0)
	v_pk_fma_f32 v[18:19], v[16:17], v[34:35], v[18:19] op_sel:[1,0,0]
	v_pk_fma_f32 v[20:21], v[16:17], v[36:37], v[20:21] op_sel:[1,0,0]
	v_pk_fma_f32 v[22:23], v[16:17], v[38:39], v[22:23] op_sel:[1,0,0]
	v_pk_fma_f32 v[24:25], v[16:17], v[40:41], v[24:25] op_sel:[1,0,0]
	v_add_f32_dpp v18, v18, v18 quad_perm:[1,0,3,2] row_mask:0xf bank_mask:0xf
	v_add_f32_dpp v19, v19, v19 quad_perm:[1,0,3,2] row_mask:0xf bank_mask:0xf
	v_add_f32_dpp v20, v20, v20 quad_perm:[1,0,3,2] row_mask:0xf bank_mask:0xf
	v_add_f32_dpp v21, v21, v21 quad_perm:[1,0,3,2] row_mask:0xf bank_mask:0xf
	v_add_f32_dpp v22, v22, v22 quad_perm:[1,0,3,2] row_mask:0xf bank_mask:0xf
	v_add_f32_dpp v23, v23, v23 quad_perm:[1,0,3,2] row_mask:0xf bank_mask:0xf
	v_add_f32_dpp v24, v24, v24 quad_perm:[1,0,3,2] row_mask:0xf bank_mask:0xf
	v_add_f32_dpp v25, v25, v25 quad_perm:[1,0,3,2] row_mask:0xf bank_mask:0xf
	v_add_f32_dpp v18, v18, v18 quad_perm:[2,3,0,1] row_mask:0xf bank_mask:0xf
	v_add_f32_dpp v19, v19, v19 quad_perm:[2,3,0,1] row_mask:0xf bank_mask:0xf
	v_add_f32_dpp v20, v20, v20 quad_perm:[2,3,0,1] row_mask:0xf bank_mask:0xf
	v_add_f32_dpp v21, v21, v21 quad_perm:[2,3,0,1] row_mask:0xf bank_mask:0xf
	v_add_f32_dpp v22, v22, v22 quad_perm:[2,3,0,1] row_mask:0xf bank_mask:0xf
	v_add_f32_dpp v23, v23, v23 quad_perm:[2,3,0,1] row_mask:0xf bank_mask:0xf
	v_add_f32_dpp v24, v24, v24 quad_perm:[2,3,0,1] row_mask:0xf bank_mask:0xf
	v_add_f32_dpp v25, v25, v25 quad_perm:[2,3,0,1] row_mask:0xf bank_mask:0xf
	v_add_f32_dpp v18, v18, v18 row_half_mirror row_mask:0xf bank_mask:0xf
	v_add_f32_dpp v19, v19, v19 row_half_mirror row_mask:0xf bank_mask:0xf
	v_add_f32_dpp v20, v20, v20 row_half_mirror row_mask:0xf bank_mask:0xf
	v_add_f32_dpp v21, v21, v21 row_half_mirror row_mask:0xf bank_mask:0xf
	v_add_f32_dpp v22, v22, v22 row_half_mirror row_mask:0xf bank_mask:0xf
	v_add_f32_dpp v23, v23, v23 row_half_mirror row_mask:0xf bank_mask:0xf
	v_add_f32_dpp v24, v24, v24 row_half_mirror row_mask:0xf bank_mask:0xf
	v_add_f32_dpp v25, v25, v25 row_half_mirror row_mask:0xf bank_mask:0xf
	v_cmp_eq_u32_e32 vcc, 0, v47
	v_lshlrev_b32_e32 v55, 4, v46
	s_and_saveexec_b64 s[2:3], vcc
	global_store_dwordx4 v55, v[18:21], s[12:13]
	global_store_dwordx4 v55, v[22:25], s[14:15]
	s_endpgm
.Lkb_nd_fill:
	s_waitcnt vmcnt(0)
	ds_write_b32 v53, v45
	s_waitcnt lgkmcnt(0)
	s_barrier
.LBB1_32:
	s_endpgm
	s_nop 0
	s_nop 0
	s_nop 0
	s_nop 0
	s_nop 0
	s_nop 0
	s_nop 0
	s_nop 0
	s_nop 0
	s_nop 0
	s_nop 0
	s_nop 0
	s_nop 0
	s_nop 0
	s_nop 0
	s_nop 0
	s_nop 0
	s_nop 0
	s_nop 0
	s_nop 0
	s_nop 0
	s_nop 0
	s_nop 0
	s_nop 0
	s_nop 0
	s_nop 0
	s_nop 0
	s_nop 0
	s_nop 0
	s_nop 0
	s_nop 0
	s_nop 0
	s_nop 0
	s_nop 0
	s_nop 0
	s_nop 0
	s_nop 0
	s_nop 0
	s_nop 0
	s_nop 0
	s_nop 0
	s_nop 0
	s_nop 0
	s_nop 0
	s_nop 0
	s_nop 0
	s_nop 0
	s_nop 0
	s_endpgm
